# attention epilogue output stores carry the nt hint (written once, not re-read in this phase)
# baseline (speedup 1.0000x reference)
; __device__ __forceinline__ unsigned pk2(float a, float b) { f32x2_t v = {a, b}; bf16x2_t r = __builtin_convertvector(v, bf16x2_t); return __builtin_bit_cast(unsigned, r); }
; template <bool MLA>
; __device__ __forceinline__ void attn_unit(const P& p, LAS unsigned char* lds, const int b, const int h, const int qb) {
;     ...
;     if (MLA) { if (hi == 0) al[r32] = 1.0f / l_run; asm volatile("s_waitcnt lgkmcnt(0)" ::: "memory"); }
;     char* Ob = (char*)(WSP(bf16_t, WS_MIXED) + (size_t)(b * SEQ + qw) * 2048 + (MLA ? 1024 : 0) + h * 128);
;     const bool odd = (r32 & 1) != 0;
;     const unsigned oo = (unsigned)((4 * hi * 2048 + r32) * 2) + (odd ? 4094u : 0u);
; #pragma unroll
;     for (int q = 0; q < 8; ++q) { const int ra = 2 * q, c = (ra & 3) + 8 * (ra >> 2); const float iva = MLA ? al[c + 4 * hi] : 1.f, ivb = MLA ? al[c + 1 + 4 * hi] : 1.f;
; #pragma unroll
;         for (int d0 = 0; d0 < 4; ++d0) { const float A = o[d0][ra] * iva, Bv = o[d0][ra + 1] * ivb;
;             const float snd = odd ? A : Bv;
;             const float rcv = __int_as_float(__builtin_amdgcn_update_dpp(0, __float_as_int(snd), 0xB1, 0xF, 0xF, true));
;             const unsigned w = odd ? pk2(rcv, Bv) : pk2(A, rcv);
;             *(unsigned*)(Ob + oo + (unsigned)((c * 2048 + d0 * 32) * 2)) = w; } }
.LBB0_696:
	s_or_b64 exec, exec, s[0:1]
	s_waitcnt lgkmcnt(0)
	v_add_u32_e32 v3, s91, v198
	ds_read_b128 v[6:9], v3
	ds_read_b128 v[10:13], v3 offset:32
	s_lshl_b64 s[0:1], s[82:83], 12
	s_add_u32 s0, s74, s0
	s_addc_u32 s1, s75, s1
	s_lshl_b32 s2, s90, 1
	s_add_u32 s0, s0, s2
	s_waitcnt lgkmcnt(1)
	v_mul_f32_e32 v16, v66, v6
	v_mul_f32_e32 v17, v67, v7
	s_addc_u32 s1, s1, 0
	v_cndmask_b32_e64 v66, v16, v17, s[6:7]
	v_lshl_add_u64 v[4:5], s[0:1], 0, v[186:187]
	s_mov_b64 s[0:1], 0x13740800
	v_mov_b32_dpp v66, v66 quad_perm:[1,0,3,2] row_mask:0xf bank_mask:0xf bound_ctrl:1
	v_lshl_add_u64 v[14:15], v[4:5], 0, s[0:1]
	v_cndmask_b32_e64 v17, v17, v66, s[6:7]
	v_cndmask_b32_e64 v16, v66, v16, s[6:7]
	s_mov_b32 s0, 0x13740000
	v_cvt_pk_bf16_f32 v66, v16, v17
	v_add_co_u32_e32 v16, vcc, s0, v4
	s_mov_b32 s0, 0x13742000
	s_nop 0
	v_addc_co_u32_e32 v17, vcc, 0, v5, vcc
	global_store_dword v[16:17], v66, off offset:2048 nt
	v_mul_f32_e32 v16, v50, v6
	v_mul_f32_e32 v17, v51, v7
	v_cndmask_b32_e64 v50, v16, v17, s[6:7]
	s_nop 1
	v_mov_b32_dpp v50, v50 quad_perm:[1,0,3,2] row_mask:0xf bank_mask:0xf bound_ctrl:1
	v_cndmask_b32_e64 v17, v17, v50, s[6:7]
	v_cndmask_b32_e64 v16, v50, v16, s[6:7]
	v_cvt_pk_bf16_f32 v16, v16, v17
	global_store_dword v[14:15], v16, off offset:64 nt
	v_mul_f32_e32 v16, v34, v6
	v_mul_f32_e32 v17, v35, v7
	v_cndmask_b32_e64 v34, v16, v17, s[6:7]
	v_mul_f32_e32 v6, v18, v6
	v_mul_f32_e32 v7, v19, v7
	v_mov_b32_dpp v34, v34 quad_perm:[1,0,3,2] row_mask:0xf bank_mask:0xf bound_ctrl:1
	v_cndmask_b32_e64 v17, v17, v34, s[6:7]
	v_cndmask_b32_e64 v16, v34, v16, s[6:7]
	v_cvt_pk_bf16_f32 v16, v16, v17
	global_store_dword v[14:15], v16, off offset:128 nt
	v_cndmask_b32_e64 v16, v6, v7, s[6:7]
	s_nop 1
	v_mov_b32_dpp v16, v16 quad_perm:[1,0,3,2] row_mask:0xf bank_mask:0xf bound_ctrl:1
	v_cndmask_b32_e64 v7, v7, v16, s[6:7]
	v_cndmask_b32_e64 v6, v16, v6, s[6:7]
	v_cvt_pk_bf16_f32 v6, v6, v7
	global_store_dword v[14:15], v6, off offset:192 nt
	v_mul_f32_e32 v6, v68, v8
	v_mul_f32_e32 v7, v69, v9
	v_cndmask_b32_e64 v14, v6, v7, s[6:7]
	v_mul_f32_e32 v15, v53, v9
	s_nop 0
	v_mov_b32_dpp v14, v14 quad_perm:[1,0,3,2] row_mask:0xf bank_mask:0xf bound_ctrl:1
	v_cndmask_b32_e64 v7, v7, v14, s[6:7]
	v_cndmask_b32_e64 v6, v14, v6, s[6:7]
	v_cvt_pk_bf16_f32 v14, v6, v7
	v_add_co_u32_e32 v6, vcc, s0, v4
	s_mov_b32 s0, 0x13748000
	s_nop 0
	v_addc_co_u32_e32 v7, vcc, 0, v5, vcc
	global_store_dword v[6:7], v14, off offset:2048 nt
	v_mul_f32_e32 v14, v52, v8
	v_cndmask_b32_e64 v16, v14, v15, s[6:7]
	s_nop 1
	v_mov_b32_dpp v16, v16 quad_perm:[1,0,3,2] row_mask:0xf bank_mask:0xf bound_ctrl:1
	v_cndmask_b32_e64 v15, v15, v16, s[6:7]
	v_cndmask_b32_e64 v14, v16, v14, s[6:7]
	v_cvt_pk_bf16_f32 v14, v14, v15
	global_store_dword v[6:7], v14, off offset:2112 nt
	v_mul_f32_e32 v14, v36, v8
	v_mul_f32_e32 v15, v37, v9
	v_cndmask_b32_e64 v16, v14, v15, s[6:7]
	v_mul_f32_e32 v8, v20, v8
	v_mul_f32_e32 v9, v21, v9
	v_mov_b32_dpp v16, v16 quad_perm:[1,0,3,2] row_mask:0xf bank_mask:0xf bound_ctrl:1
	v_cndmask_b32_e64 v15, v15, v16, s[6:7]
	v_cndmask_b32_e64 v14, v16, v14, s[6:7]
	v_cvt_pk_bf16_f32 v14, v14, v15
	global_store_dword v[6:7], v14, off offset:2176 nt
	v_cndmask_b32_e64 v14, v8, v9, s[6:7]
	s_nop 1
	v_mov_b32_dpp v14, v14 quad_perm:[1,0,3,2] row_mask:0xf bank_mask:0xf bound_ctrl:1
	v_cndmask_b32_e64 v9, v9, v14, s[6:7]
	v_cndmask_b32_e64 v8, v14, v8, s[6:7]
	v_cvt_pk_bf16_f32 v8, v8, v9
	global_store_dword v[6:7], v8, off offset:2240 nt
	s_waitcnt lgkmcnt(0)
	v_mul_f32_e32 v6, v70, v10
	v_mul_f32_e32 v7, v71, v11
	v_cndmask_b32_e64 v8, v6, v7, s[6:7]
	v_mul_f32_e32 v9, v55, v11
	s_nop 0
	v_mov_b32_dpp v8, v8 quad_perm:[1,0,3,2] row_mask:0xf bank_mask:0xf bound_ctrl:1
	v_cndmask_b32_e64 v7, v7, v8, s[6:7]
	v_cndmask_b32_e64 v6, v8, v6, s[6:7]
	v_cvt_pk_bf16_f32 v8, v6, v7
	v_add_co_u32_e32 v6, vcc, s0, v4
	s_mov_b32 s0, 0x1374a000
	s_nop 0
	v_addc_co_u32_e32 v7, vcc, 0, v5, vcc
	global_store_dword v[6:7], v8, off offset:2048 nt
	v_mul_f32_e32 v8, v54, v10
	v_cndmask_b32_e64 v14, v8, v9, s[6:7]
	s_nop 1
	v_mov_b32_dpp v14, v14 quad_perm:[1,0,3,2] row_mask:0xf bank_mask:0xf bound_ctrl:1
	v_cndmask_b32_e64 v9, v9, v14, s[6:7]
	v_cndmask_b32_e64 v8, v14, v8, s[6:7]
	v_cvt_pk_bf16_f32 v8, v8, v9
	global_store_dword v[6:7], v8, off offset:2112 nt
	v_mul_f32_e32 v8, v38, v10
	v_mul_f32_e32 v9, v39, v11
	v_cndmask_b32_e64 v14, v8, v9, s[6:7]
	s_nop 1
	v_mov_b32_dpp v14, v14 quad_perm:[1,0,3,2] row_mask:0xf bank_mask:0xf bound_ctrl:1
	v_cndmask_b32_e64 v9, v9, v14, s[6:7]
	v_cndmask_b32_e64 v8, v14, v8, s[6:7]
	v_cvt_pk_bf16_f32 v8, v8, v9
	global_store_dword v[6:7], v8, off offset:2176 nt
	v_mul_f32_e32 v8, v22, v10
	v_mul_f32_e32 v9, v23, v11
	v_cndmask_b32_e64 v10, v8, v9, s[6:7]
	s_nop 1
	v_mov_b32_dpp v10, v10 quad_perm:[1,0,3,2] row_mask:0xf bank_mask:0xf bound_ctrl:1
	v_cndmask_b32_e64 v9, v9, v10, s[6:7]
	v_cndmask_b32_e64 v8, v10, v8, s[6:7]
	v_cvt_pk_bf16_f32 v8, v8, v9
	global_store_dword v[6:7], v8, off offset:2240 nt
	v_mul_f32_e32 v6, v72, v12
	v_mul_f32_e32 v7, v73, v13
	v_cndmask_b32_e64 v8, v6, v7, s[6:7]
	v_add_co_u32_e32 v10, vcc, s0, v4
	s_nop 0
	v_mov_b32_dpp v8, v8 quad_perm:[1,0,3,2] row_mask:0xf bank_mask:0xf bound_ctrl:1
	v_cndmask_b32_e64 v7, v7, v8, s[6:7]
	v_cndmask_b32_e64 v6, v8, v6, s[6:7]
	v_cvt_pk_bf16_f32 v6, v6, v7
	v_addc_co_u32_e32 v11, vcc, 0, v5, vcc
	global_store_dword v[10:11], v6, off offset:2048 nt
	v_mul_f32_e32 v6, v56, v12
	v_mul_f32_e32 v7, v57, v13
	v_cndmask_b32_e64 v8, v6, v7, s[6:7]
	s_mov_b32 s0, 0x13750000
	s_nop 0
	v_mov_b32_dpp v8, v8 quad_perm:[1,0,3,2] row_mask:0xf bank_mask:0xf bound_ctrl:1
	v_cndmask_b32_e64 v7, v7, v8, s[6:7]
	v_cndmask_b32_e64 v6, v8, v6, s[6:7]
	v_cvt_pk_bf16_f32 v6, v6, v7
	global_store_dword v[10:11], v6, off offset:2112 nt
	v_mul_f32_e32 v6, v40, v12
	v_mul_f32_e32 v7, v41, v13
	v_cndmask_b32_e64 v8, v6, v7, s[6:7]
	v_mul_f32_e32 v12, v24, v12
	s_nop 0
	v_mov_b32_dpp v8, v8 quad_perm:[1,0,3,2] row_mask:0xf bank_mask:0xf bound_ctrl:1
	v_cndmask_b32_e64 v7, v7, v8, s[6:7]
	v_cndmask_b32_e64 v6, v8, v6, s[6:7]
	v_cvt_pk_bf16_f32 v6, v6, v7
	global_store_dword v[10:11], v6, off offset:2176 nt
	v_mul_f32_e32 v6, v25, v13
	v_cndmask_b32_e64 v7, v12, v6, s[6:7]
	s_nop 1
	v_mov_b32_dpp v13, v7 quad_perm:[1,0,3,2] row_mask:0xf bank_mask:0xf bound_ctrl:1
	v_cndmask_b32_e64 v14, v6, v13, s[6:7]
	ds_read_b128 v[6:9], v3 offset:64
	v_cndmask_b32_e64 v12, v13, v12, s[6:7]
	v_cvt_pk_bf16_f32 v12, v12, v14
	global_store_dword v[10:11], v12, off offset:2240 nt
	ds_read_b128 v[10:13], v3 offset:96
	s_waitcnt lgkmcnt(1)
; __device__ __forceinline__ unsigned pk2(float a, float b) { f32x2_t v = {a, b}; bf16x2_t r = __builtin_convertvector(v, bf16x2_t); return __builtin_bit_cast(unsigned, r); }
; template <bool MLA>
; __device__ __forceinline__ void attn_unit(const P& p, LAS unsigned char* lds, const int b, const int h, const int qb) {
;     ...
; #pragma unroll
;     for (int q = 0; q < 8; ++q) { const int ra = 2 * q, c = (ra & 3) + 8 * (ra >> 2); const float iva = MLA ? al[c + 4 * hi] : 1.f, ivb = MLA ? al[c + 1 + 4 * hi] : 1.f;
; #pragma unroll
;         for (int d0 = 0; d0 < 4; ++d0) { const float A = o[d0][ra] * iva, Bv = o[d0][ra + 1] * ivb;
;             const float snd = odd ? A : Bv;
;             const float rcv = __int_as_float(__builtin_amdgcn_update_dpp(0, __float_as_int(snd), 0xB1, 0xF, 0xF, true));
;             const unsigned w = odd ? pk2(rcv, Bv) : pk2(A, rcv);
;             *(unsigned*)(Ob + oo + (unsigned)((c * 2048 + d0 * 32) * 2)) = w; } }
;     __syncthreads();
; __device__ __forceinline__ void attn_queues(const P& p, LAS unsigned char* lds, int* ctr, const int xg) {
;     ...
;             v = qs[0];
	v_mul_f32_e32 v3, v74, v6
	v_mul_f32_e32 v14, v75, v7
	v_cndmask_b32_e64 v15, v3, v14, s[6:7]
	v_mul_f32_e32 v16, v59, v7
	s_nop 0
	v_mov_b32_dpp v15, v15 quad_perm:[1,0,3,2] row_mask:0xf bank_mask:0xf bound_ctrl:1
	v_cndmask_b32_e64 v14, v14, v15, s[6:7]
	v_cndmask_b32_e64 v3, v15, v3, s[6:7]
	v_cvt_pk_bf16_f32 v3, v3, v14
	v_add_co_u32_e32 v14, vcc, s0, v4
	s_mov_b32 s0, 0x13752000
	s_nop 0
	v_addc_co_u32_e32 v15, vcc, 0, v5, vcc
	global_store_dword v[14:15], v3, off offset:2048 nt
	v_mul_f32_e32 v3, v58, v6
	v_cndmask_b32_e64 v17, v3, v16, s[6:7]
	s_nop 1
	v_mov_b32_dpp v17, v17 quad_perm:[1,0,3,2] row_mask:0xf bank_mask:0xf bound_ctrl:1
	v_cndmask_b32_e64 v16, v16, v17, s[6:7]
	v_cndmask_b32_e64 v3, v17, v3, s[6:7]
	v_cvt_pk_bf16_f32 v3, v3, v16
	global_store_dword v[14:15], v3, off offset:2112 nt
	v_mul_f32_e32 v3, v42, v6
	v_mul_f32_e32 v16, v43, v7
	v_cndmask_b32_e64 v17, v3, v16, s[6:7]
	s_nop 1
	v_mov_b32_dpp v17, v17 quad_perm:[1,0,3,2] row_mask:0xf bank_mask:0xf bound_ctrl:1
	v_cndmask_b32_e64 v16, v16, v17, s[6:7]
	v_cndmask_b32_e64 v3, v17, v3, s[6:7]
	v_cvt_pk_bf16_f32 v3, v3, v16
	global_store_dword v[14:15], v3, off offset:2176 nt
	v_mul_f32_e32 v3, v26, v6
	v_mul_f32_e32 v6, v27, v7
	v_cndmask_b32_e64 v7, v3, v6, s[6:7]
	s_nop 1
	v_mov_b32_dpp v7, v7 quad_perm:[1,0,3,2] row_mask:0xf bank_mask:0xf bound_ctrl:1
	v_cndmask_b32_e64 v6, v6, v7, s[6:7]
	v_cndmask_b32_e64 v3, v7, v3, s[6:7]
	v_cvt_pk_bf16_f32 v3, v3, v6
	global_store_dword v[14:15], v3, off offset:2240 nt
	v_mul_f32_e32 v3, v76, v8
	v_mul_f32_e32 v6, v77, v9
	v_cndmask_b32_e64 v7, v3, v6, s[6:7]
	v_mul_f32_e32 v14, v61, v9
	s_nop 0
	v_mov_b32_dpp v7, v7 quad_perm:[1,0,3,2] row_mask:0xf bank_mask:0xf bound_ctrl:1
	v_cndmask_b32_e64 v6, v6, v7, s[6:7]
	v_cndmask_b32_e64 v3, v7, v3, s[6:7]
	v_cvt_pk_bf16_f32 v3, v3, v6
	v_add_co_u32_e32 v6, vcc, s0, v4
	s_mov_b32 s0, 0x13758000
	s_nop 0
	v_addc_co_u32_e32 v7, vcc, 0, v5, vcc
	global_store_dword v[6:7], v3, off offset:2048 nt
	v_mul_f32_e32 v3, v60, v8
	v_cndmask_b32_e64 v15, v3, v14, s[6:7]
	s_nop 1
	v_mov_b32_dpp v15, v15 quad_perm:[1,0,3,2] row_mask:0xf bank_mask:0xf bound_ctrl:1
	v_cndmask_b32_e64 v14, v14, v15, s[6:7]
	v_cndmask_b32_e64 v3, v15, v3, s[6:7]
	v_cvt_pk_bf16_f32 v3, v3, v14
	global_store_dword v[6:7], v3, off offset:2112 nt
	v_mul_f32_e32 v3, v44, v8
	v_mul_f32_e32 v14, v45, v9
	v_cndmask_b32_e64 v15, v3, v14, s[6:7]
	s_nop 1
	v_mov_b32_dpp v15, v15 quad_perm:[1,0,3,2] row_mask:0xf bank_mask:0xf bound_ctrl:1
	v_cndmask_b32_e64 v14, v14, v15, s[6:7]
	v_cndmask_b32_e64 v3, v15, v3, s[6:7]
	v_cvt_pk_bf16_f32 v3, v3, v14
	global_store_dword v[6:7], v3, off offset:2176 nt
	v_mul_f32_e32 v3, v28, v8
	v_mul_f32_e32 v8, v29, v9
	v_cndmask_b32_e64 v9, v3, v8, s[6:7]
	s_nop 1
	v_mov_b32_dpp v9, v9 quad_perm:[1,0,3,2] row_mask:0xf bank_mask:0xf bound_ctrl:1
	v_cndmask_b32_e64 v8, v8, v9, s[6:7]
	v_cndmask_b32_e64 v3, v9, v3, s[6:7]
	v_cvt_pk_bf16_f32 v3, v3, v8
	global_store_dword v[6:7], v3, off offset:2240 nt
	s_waitcnt lgkmcnt(0)
	v_mul_f32_e32 v3, v78, v10
	v_mul_f32_e32 v6, v79, v11
	v_cndmask_b32_e64 v7, v3, v6, s[6:7]
	v_mul_f32_e32 v8, v63, v11
	s_nop 0
	v_mov_b32_dpp v7, v7 quad_perm:[1,0,3,2] row_mask:0xf bank_mask:0xf bound_ctrl:1
	v_cndmask_b32_e64 v6, v6, v7, s[6:7]
	v_cndmask_b32_e64 v3, v7, v3, s[6:7]
	v_cvt_pk_bf16_f32 v3, v3, v6
	v_add_co_u32_e32 v6, vcc, s0, v4
	s_mov_b32 s0, 0x1375a000
	s_nop 0
	v_addc_co_u32_e32 v7, vcc, 0, v5, vcc
	global_store_dword v[6:7], v3, off offset:2048 nt
	v_mul_f32_e32 v3, v62, v10
	v_cndmask_b32_e64 v9, v3, v8, s[6:7]
	v_add_co_u32_e32 v4, vcc, s0, v4
	s_nop 0
	v_mov_b32_dpp v9, v9 quad_perm:[1,0,3,2] row_mask:0xf bank_mask:0xf bound_ctrl:1
	v_cndmask_b32_e64 v8, v8, v9, s[6:7]
	v_cndmask_b32_e64 v3, v9, v3, s[6:7]
	v_cvt_pk_bf16_f32 v3, v3, v8
	global_store_dword v[6:7], v3, off offset:2112 nt
	v_mul_f32_e32 v3, v46, v10
	v_mul_f32_e32 v8, v47, v11
	v_cndmask_b32_e64 v9, v3, v8, s[6:7]
	v_addc_co_u32_e32 v5, vcc, 0, v5, vcc
	s_nop 0
	v_mov_b32_dpp v9, v9 quad_perm:[1,0,3,2] row_mask:0xf bank_mask:0xf bound_ctrl:1
	v_cndmask_b32_e64 v8, v8, v9, s[6:7]
	v_cndmask_b32_e64 v3, v9, v3, s[6:7]
	v_cvt_pk_bf16_f32 v3, v3, v8
	global_store_dword v[6:7], v3, off offset:2176 nt
	v_mul_f32_e32 v3, v30, v10
	v_mul_f32_e32 v8, v31, v11
	v_cndmask_b32_e64 v9, v3, v8, s[6:7]
	s_nop 1
	v_mov_b32_dpp v9, v9 quad_perm:[1,0,3,2] row_mask:0xf bank_mask:0xf bound_ctrl:1
	v_cndmask_b32_e64 v8, v8, v9, s[6:7]
	v_cndmask_b32_e64 v3, v9, v3, s[6:7]
	v_cvt_pk_bf16_f32 v3, v3, v8
	global_store_dword v[6:7], v3, off offset:2240 nt
	v_mul_f32_e32 v3, v80, v12
	v_mul_f32_e32 v6, v81, v13
	v_cndmask_b32_e64 v7, v3, v6, s[6:7]
	s_nop 1
	v_mov_b32_dpp v7, v7 quad_perm:[1,0,3,2] row_mask:0xf bank_mask:0xf bound_ctrl:1
	v_cndmask_b32_e64 v6, v6, v7, s[6:7]
	v_cndmask_b32_e64 v3, v7, v3, s[6:7]
	v_cvt_pk_bf16_f32 v3, v3, v6
	global_store_dword v[4:5], v3, off offset:2048 nt
	v_mul_f32_e32 v3, v64, v12
	v_mul_f32_e32 v6, v65, v13
	v_cndmask_b32_e64 v7, v3, v6, s[6:7]
	s_nop 1
	v_mov_b32_dpp v7, v7 quad_perm:[1,0,3,2] row_mask:0xf bank_mask:0xf bound_ctrl:1
	v_cndmask_b32_e64 v6, v6, v7, s[6:7]
	v_cndmask_b32_e64 v3, v7, v3, s[6:7]
	v_cvt_pk_bf16_f32 v3, v3, v6
	global_store_dword v[4:5], v3, off offset:2112 nt
	v_mul_f32_e32 v3, v48, v12
	v_mul_f32_e32 v6, v49, v13
	v_cndmask_b32_e64 v7, v3, v6, s[6:7]
	s_nop 1
	v_mov_b32_dpp v7, v7 quad_perm:[1,0,3,2] row_mask:0xf bank_mask:0xf bound_ctrl:1
	v_cndmask_b32_e64 v6, v6, v7, s[6:7]
	v_cndmask_b32_e64 v3, v7, v3, s[6:7]
	v_cvt_pk_bf16_f32 v3, v3, v6
	global_store_dword v[4:5], v3, off offset:2176 nt
	v_mul_f32_e32 v3, v32, v12
	v_mul_f32_e32 v6, v33, v13
	v_cndmask_b32_e64 v7, v3, v6, s[6:7]
	s_nop 1
	v_mov_b32_dpp v7, v7 quad_perm:[1,0,3,2] row_mask:0xf bank_mask:0xf bound_ctrl:1
	v_cndmask_b32_e64 v6, v6, v7, s[6:7]
	v_cndmask_b32_e64 v3, v7, v3, s[6:7]
	v_cvt_pk_bf16_f32 v3, v3, v6
	global_store_dword v[4:5], v3, off offset:2240 nt
	v_mov_b32_e32 v3, s40
	s_barrier
	ds_read_b32 v3, v3
	s_waitcnt lgkmcnt(0)
	v_cmp_gt_i32_e32 vcc, s3, v3
	v_readfirstlane_b32 s2, v3
	s_cbranch_vccz .LBB0_722

; __device__ __forceinline__ unsigned pk2(float a, float b) { f32x2_t v = {a, b}; bf16x2_t r = __builtin_convertvector(v, bf16x2_t); return __builtin_bit_cast(unsigned, r); }
; template <bool MLA>
; __device__ __forceinline__ void attn_unit(const P& p, LAS unsigned char* lds, const int b, const int h, const int qb) {
;     ...
;     char* Ob = (char*)(WSP(bf16_t, WS_MIXED) + (size_t)(b * SEQ + qw) * 2048 + (MLA ? 1024 : 0) + h * 128);
;     const bool odd = (r32 & 1) != 0;
;     const unsigned oo = (unsigned)((4 * hi * 2048 + r32) * 2) + (odd ? 4094u : 0u);
; #pragma unroll
;     for (int q = 0; q < 8; ++q) { const int ra = 2 * q, c = (ra & 3) + 8 * (ra >> 2); const float iva = MLA ? al[c + 4 * hi] : 1.f, ivb = MLA ? al[c + 1 + 4 * hi] : 1.f;
; #pragma unroll
;         for (int d0 = 0; d0 < 4; ++d0) { const float A = o[d0][ra] * iva, Bv = o[d0][ra + 1] * ivb;
;             const float snd = odd ? A : Bv;
;             const float rcv = __int_as_float(__builtin_amdgcn_update_dpp(0, __float_as_int(snd), 0xB1, 0xF, 0xF, true));
;             const unsigned w = odd ? pk2(rcv, Bv) : pk2(A, rcv);
;             *(unsigned*)(Ob + oo + (unsigned)((c * 2048 + d0 * 32) * 2)) = w; } }
;     __syncthreads();
.LBB0_729:
	s_lshl_b64 s[0:1], s[96:97], 12
	s_add_u32 s0, s90, s0
	s_addc_u32 s1, s91, s1
	v_cndmask_b32_e64 v3, v66, v67, s[8:9]
	s_add_u32 s0, s0, s33
	s_addc_u32 s1, s1, 0
	v_mov_b32_dpp v3, v3 quad_perm:[1,0,3,2] row_mask:0xf bank_mask:0xf bound_ctrl:1
	v_cndmask_b32_e64 v6, v67, v3, s[8:9]
	v_cndmask_b32_e64 v3, v3, v66, s[8:9]
	v_lshl_add_u64 v[4:5], s[0:1], 0, v[176:177]
	v_cvt_pk_bf16_f32 v3, v3, v6
	s_barrier
	global_store_dword v[4:5], v3, off nt
	v_cndmask_b32_e64 v3, v34, v35, s[8:9]
	s_movk_i32 s0, 0x2000
	s_mov_b32 s20, 0x10000
	v_mov_b32_dpp v3, v3 quad_perm:[1,0,3,2] row_mask:0xf bank_mask:0xf bound_ctrl:1
	v_cndmask_b32_e64 v6, v35, v3, s[8:9]
	v_cndmask_b32_e64 v3, v3, v34, s[8:9]
	v_cvt_pk_bf16_f32 v3, v3, v6
	global_store_dword v[4:5], v3, off offset:64 nt
	v_cndmask_b32_e64 v3, v18, v19, s[8:9]
	s_nop 1
	v_mov_b32_dpp v3, v3 quad_perm:[1,0,3,2] row_mask:0xf bank_mask:0xf bound_ctrl:1
	v_cndmask_b32_e64 v6, v19, v3, s[8:9]
	v_cndmask_b32_e64 v3, v3, v18, s[8:9]
	v_cvt_pk_bf16_f32 v3, v3, v6
	global_store_dword v[4:5], v3, off offset:128 nt
	v_cndmask_b32_e64 v3, v50, v51, s[8:9]
	s_nop 1
	v_mov_b32_dpp v3, v3 quad_perm:[1,0,3,2] row_mask:0xf bank_mask:0xf bound_ctrl:1
	v_cndmask_b32_e64 v6, v51, v3, s[8:9]
	v_cndmask_b32_e64 v3, v3, v50, s[8:9]
	v_cvt_pk_bf16_f32 v3, v3, v6
	global_store_dword v[4:5], v3, off offset:192 nt
	v_cndmask_b32_e64 v3, v68, v69, s[8:9]
	s_nop 1
	v_mov_b32_dpp v3, v3 quad_perm:[1,0,3,2] row_mask:0xf bank_mask:0xf bound_ctrl:1
	v_cndmask_b32_e64 v6, v69, v3, s[8:9]
	v_cndmask_b32_e64 v3, v3, v68, s[8:9]
	v_cvt_pk_bf16_f32 v3, v3, v6
	v_add_co_u32_e32 v6, vcc, s0, v4
	s_mov_b32 s0, 0x8000
	s_nop 0
	v_addc_co_u32_e32 v7, vcc, 0, v5, vcc
	global_store_dword v[6:7], v3, off nt
	v_cndmask_b32_e64 v3, v36, v37, s[8:9]
	s_nop 1
	v_mov_b32_dpp v3, v3 quad_perm:[1,0,3,2] row_mask:0xf bank_mask:0xf bound_ctrl:1
	v_cndmask_b32_e64 v8, v37, v3, s[8:9]
	v_cndmask_b32_e64 v3, v3, v36, s[8:9]
	v_cvt_pk_bf16_f32 v3, v3, v8
	global_store_dword v[6:7], v3, off offset:64 nt
	v_cndmask_b32_e64 v3, v20, v21, s[8:9]
	s_nop 1
	v_mov_b32_dpp v3, v3 quad_perm:[1,0,3,2] row_mask:0xf bank_mask:0xf bound_ctrl:1
	v_cndmask_b32_e64 v8, v21, v3, s[8:9]
	v_cndmask_b32_e64 v3, v3, v20, s[8:9]
	v_cvt_pk_bf16_f32 v3, v3, v8
	global_store_dword v[6:7], v3, off offset:128 nt
	v_cndmask_b32_e64 v3, v52, v53, s[8:9]
	s_nop 1
	v_mov_b32_dpp v3, v3 quad_perm:[1,0,3,2] row_mask:0xf bank_mask:0xf bound_ctrl:1
	v_cndmask_b32_e64 v8, v53, v3, s[8:9]
	v_cndmask_b32_e64 v3, v3, v52, s[8:9]
	v_cvt_pk_bf16_f32 v3, v3, v8
	global_store_dword v[6:7], v3, off offset:192 nt
	v_cndmask_b32_e64 v3, v70, v71, s[8:9]
	s_nop 1
	v_mov_b32_dpp v3, v3 quad_perm:[1,0,3,2] row_mask:0xf bank_mask:0xf bound_ctrl:1
	v_cndmask_b32_e64 v6, v71, v3, s[8:9]
	v_cndmask_b32_e64 v3, v3, v70, s[8:9]
	v_cvt_pk_bf16_f32 v3, v3, v6
	v_add_co_u32_e32 v6, vcc, s0, v4
	s_mov_b32 s0, 0xa000
	s_nop 0
	v_addc_co_u32_e32 v7, vcc, 0, v5, vcc
	global_store_dword v[6:7], v3, off nt
	v_cndmask_b32_e64 v3, v38, v39, s[8:9]
	s_nop 1
	v_mov_b32_dpp v3, v3 quad_perm:[1,0,3,2] row_mask:0xf bank_mask:0xf bound_ctrl:1
	v_cndmask_b32_e64 v8, v39, v3, s[8:9]
	v_cndmask_b32_e64 v3, v3, v38, s[8:9]
	v_cvt_pk_bf16_f32 v3, v3, v8
	global_store_dword v[6:7], v3, off offset:64 nt
	v_cndmask_b32_e64 v3, v22, v23, s[8:9]
	s_nop 1
	v_mov_b32_dpp v3, v3 quad_perm:[1,0,3,2] row_mask:0xf bank_mask:0xf bound_ctrl:1
	v_cndmask_b32_e64 v8, v23, v3, s[8:9]
	v_cndmask_b32_e64 v3, v3, v22, s[8:9]
	v_cvt_pk_bf16_f32 v3, v3, v8
	global_store_dword v[6:7], v3, off offset:128 nt
	v_cndmask_b32_e64 v3, v54, v55, s[8:9]
	s_nop 1
	v_mov_b32_dpp v3, v3 quad_perm:[1,0,3,2] row_mask:0xf bank_mask:0xf bound_ctrl:1
	v_cndmask_b32_e64 v8, v55, v3, s[8:9]
	v_cndmask_b32_e64 v3, v3, v54, s[8:9]
	v_cvt_pk_bf16_f32 v3, v3, v8
	global_store_dword v[6:7], v3, off offset:192 nt
	v_cndmask_b32_e64 v3, v72, v73, s[8:9]
	s_nop 1
	v_mov_b32_dpp v3, v3 quad_perm:[1,0,3,2] row_mask:0xf bank_mask:0xf bound_ctrl:1
	v_cndmask_b32_e64 v6, v73, v3, s[8:9]
	v_cndmask_b32_e64 v3, v3, v72, s[8:9]
	v_cvt_pk_bf16_f32 v3, v3, v6
	v_add_co_u32_e32 v6, vcc, s0, v4
	s_mov_b32 s0, 0x12000
	s_nop 0
	v_addc_co_u32_e32 v7, vcc, 0, v5, vcc
	global_store_dword v[6:7], v3, off nt
	v_cndmask_b32_e64 v3, v40, v41, s[8:9]
	s_nop 1
	v_mov_b32_dpp v3, v3 quad_perm:[1,0,3,2] row_mask:0xf bank_mask:0xf bound_ctrl:1
	v_cndmask_b32_e64 v8, v41, v3, s[8:9]
	v_cndmask_b32_e64 v3, v3, v40, s[8:9]
	v_cvt_pk_bf16_f32 v3, v3, v8
	global_store_dword v[6:7], v3, off offset:64 nt
	v_cndmask_b32_e64 v3, v24, v25, s[8:9]
	s_nop 1
	v_mov_b32_dpp v3, v3 quad_perm:[1,0,3,2] row_mask:0xf bank_mask:0xf bound_ctrl:1
	v_cndmask_b32_e64 v8, v25, v3, s[8:9]
	v_cndmask_b32_e64 v3, v3, v24, s[8:9]
	v_cvt_pk_bf16_f32 v3, v3, v8
	global_store_dword v[6:7], v3, off offset:128 nt
	v_cndmask_b32_e64 v3, v56, v57, s[8:9]
	s_nop 1
	v_mov_b32_dpp v3, v3 quad_perm:[1,0,3,2] row_mask:0xf bank_mask:0xf bound_ctrl:1
	v_cndmask_b32_e64 v8, v57, v3, s[8:9]
	v_cndmask_b32_e64 v3, v3, v56, s[8:9]
	v_cvt_pk_bf16_f32 v3, v3, v8
	global_store_dword v[6:7], v3, off offset:192 nt
; __device__ __forceinline__ unsigned pk2(float a, float b) { f32x2_t v = {a, b}; bf16x2_t r = __builtin_convertvector(v, bf16x2_t); return __builtin_bit_cast(unsigned, r); }
; template <bool MLA>
; __device__ __forceinline__ void attn_unit(const P& p, LAS unsigned char* lds, const int b, const int h, const int qb) {
;     ...
; #pragma unroll
;     for (int q = 0; q < 8; ++q) { const int ra = 2 * q, c = (ra & 3) + 8 * (ra >> 2); const float iva = MLA ? al[c + 4 * hi] : 1.f, ivb = MLA ? al[c + 1 + 4 * hi] : 1.f;
; #pragma unroll
;         for (int d0 = 0; d0 < 4; ++d0) { const float A = o[d0][ra] * iva, Bv = o[d0][ra + 1] * ivb;
;             const float snd = odd ? A : Bv;
;             const float rcv = __int_as_float(__builtin_amdgcn_update_dpp(0, __float_as_int(snd), 0xB1, 0xF, 0xF, true));
;             const unsigned w = odd ? pk2(rcv, Bv) : pk2(A, rcv);
;             *(unsigned*)(Ob + oo + (unsigned)((c * 2048 + d0 * 32) * 2)) = w; } }
;     __syncthreads();
; __device__ __forceinline__ void attn_queues(const P& p, LAS unsigned char* lds, int* ctr, const int xg) {
;     ...
;             v = qs[0];
	v_cndmask_b32_e64 v3, v74, v75, s[8:9]
	s_nop 1
	v_mov_b32_dpp v3, v3 quad_perm:[1,0,3,2] row_mask:0xf bank_mask:0xf bound_ctrl:1
	v_cndmask_b32_e64 v6, v75, v3, s[8:9]
	v_cndmask_b32_e64 v3, v3, v74, s[8:9]
	v_cvt_pk_bf16_f32 v3, v3, v6
	v_add_co_u32_e32 v6, vcc, s20, v4
	s_nop 1
	v_addc_co_u32_e32 v7, vcc, 0, v5, vcc
	global_store_dword v[6:7], v3, off nt
	v_cndmask_b32_e64 v3, v42, v43, s[8:9]
	s_nop 1
	v_mov_b32_dpp v3, v3 quad_perm:[1,0,3,2] row_mask:0xf bank_mask:0xf bound_ctrl:1
	v_cndmask_b32_e64 v8, v43, v3, s[8:9]
	v_cndmask_b32_e64 v3, v3, v42, s[8:9]
	v_cvt_pk_bf16_f32 v3, v3, v8
	global_store_dword v[6:7], v3, off offset:64 nt
	v_cndmask_b32_e64 v3, v26, v27, s[8:9]
	s_nop 1
	v_mov_b32_dpp v3, v3 quad_perm:[1,0,3,2] row_mask:0xf bank_mask:0xf bound_ctrl:1
	v_cndmask_b32_e64 v8, v27, v3, s[8:9]
	v_cndmask_b32_e64 v3, v3, v26, s[8:9]
	v_cvt_pk_bf16_f32 v3, v3, v8
	global_store_dword v[6:7], v3, off offset:128 nt
	v_cndmask_b32_e64 v3, v58, v59, s[8:9]
	s_nop 1
	v_mov_b32_dpp v3, v3 quad_perm:[1,0,3,2] row_mask:0xf bank_mask:0xf bound_ctrl:1
	v_cndmask_b32_e64 v8, v59, v3, s[8:9]
	v_cndmask_b32_e64 v3, v3, v58, s[8:9]
	v_cvt_pk_bf16_f32 v3, v3, v8
	global_store_dword v[6:7], v3, off offset:192 nt
	v_cndmask_b32_e64 v3, v76, v77, s[8:9]
	s_nop 1
	v_mov_b32_dpp v3, v3 quad_perm:[1,0,3,2] row_mask:0xf bank_mask:0xf bound_ctrl:1
	v_cndmask_b32_e64 v6, v77, v3, s[8:9]
	v_cndmask_b32_e64 v3, v3, v76, s[8:9]
	v_cvt_pk_bf16_f32 v3, v3, v6
	v_add_co_u32_e32 v6, vcc, s0, v4
	s_mov_b32 s0, 0x18000
	s_nop 0
	v_addc_co_u32_e32 v7, vcc, 0, v5, vcc
	global_store_dword v[6:7], v3, off nt
	v_cndmask_b32_e64 v3, v44, v45, s[8:9]
	s_nop 1
	v_mov_b32_dpp v3, v3 quad_perm:[1,0,3,2] row_mask:0xf bank_mask:0xf bound_ctrl:1
	v_cndmask_b32_e64 v8, v45, v3, s[8:9]
	v_cndmask_b32_e64 v3, v3, v44, s[8:9]
	v_cvt_pk_bf16_f32 v3, v3, v8
	global_store_dword v[6:7], v3, off offset:64 nt
	v_cndmask_b32_e64 v3, v28, v29, s[8:9]
	s_nop 1
	v_mov_b32_dpp v3, v3 quad_perm:[1,0,3,2] row_mask:0xf bank_mask:0xf bound_ctrl:1
	v_cndmask_b32_e64 v8, v29, v3, s[8:9]
	v_cndmask_b32_e64 v3, v3, v28, s[8:9]
	v_cvt_pk_bf16_f32 v3, v3, v8
	global_store_dword v[6:7], v3, off offset:128 nt
	v_cndmask_b32_e64 v3, v60, v61, s[8:9]
	s_nop 1
	v_mov_b32_dpp v3, v3 quad_perm:[1,0,3,2] row_mask:0xf bank_mask:0xf bound_ctrl:1
	v_cndmask_b32_e64 v8, v61, v3, s[8:9]
	v_cndmask_b32_e64 v3, v3, v60, s[8:9]
	v_cvt_pk_bf16_f32 v3, v3, v8
	global_store_dword v[6:7], v3, off offset:192 nt
	v_cndmask_b32_e64 v3, v78, v79, s[8:9]
	s_nop 1
	v_mov_b32_dpp v3, v3 quad_perm:[1,0,3,2] row_mask:0xf bank_mask:0xf bound_ctrl:1
	v_cndmask_b32_e64 v6, v79, v3, s[8:9]
	v_cndmask_b32_e64 v3, v3, v78, s[8:9]
	v_cvt_pk_bf16_f32 v3, v3, v6
	v_add_co_u32_e32 v6, vcc, s0, v4
	s_mov_b32 s0, 0x1a000
	s_nop 0
	v_addc_co_u32_e32 v7, vcc, 0, v5, vcc
	global_store_dword v[6:7], v3, off nt
	v_cndmask_b32_e64 v3, v46, v47, s[8:9]
	v_add_co_u32_e32 v4, vcc, s0, v4
	s_nop 0
	v_mov_b32_dpp v3, v3 quad_perm:[1,0,3,2] row_mask:0xf bank_mask:0xf bound_ctrl:1
	v_cndmask_b32_e64 v8, v47, v3, s[8:9]
	v_cndmask_b32_e64 v3, v3, v46, s[8:9]
	v_cvt_pk_bf16_f32 v3, v3, v8
	global_store_dword v[6:7], v3, off offset:64 nt
	v_cndmask_b32_e64 v3, v30, v31, s[8:9]
	v_addc_co_u32_e32 v5, vcc, 0, v5, vcc
	s_nop 0
	v_mov_b32_dpp v3, v3 quad_perm:[1,0,3,2] row_mask:0xf bank_mask:0xf bound_ctrl:1
	v_cndmask_b32_e64 v8, v31, v3, s[8:9]
	v_cndmask_b32_e64 v3, v3, v30, s[8:9]
	v_cvt_pk_bf16_f32 v3, v3, v8
	global_store_dword v[6:7], v3, off offset:128 nt
	v_cndmask_b32_e64 v3, v62, v63, s[8:9]
	s_nop 1
	v_mov_b32_dpp v3, v3 quad_perm:[1,0,3,2] row_mask:0xf bank_mask:0xf bound_ctrl:1
	v_cndmask_b32_e64 v8, v63, v3, s[8:9]
	v_cndmask_b32_e64 v3, v3, v62, s[8:9]
	v_cvt_pk_bf16_f32 v3, v3, v8
	global_store_dword v[6:7], v3, off offset:192 nt
	v_cndmask_b32_e64 v3, v80, v81, s[8:9]
	s_nop 1
	v_mov_b32_dpp v3, v3 quad_perm:[1,0,3,2] row_mask:0xf bank_mask:0xf bound_ctrl:1
	v_cndmask_b32_e64 v6, v81, v3, s[8:9]
	v_cndmask_b32_e64 v3, v3, v80, s[8:9]
	v_cvt_pk_bf16_f32 v3, v3, v6
	global_store_dword v[4:5], v3, off nt
	v_cndmask_b32_e64 v3, v48, v49, s[8:9]
	s_nop 1
	v_mov_b32_dpp v3, v3 quad_perm:[1,0,3,2] row_mask:0xf bank_mask:0xf bound_ctrl:1
	v_cndmask_b32_e64 v6, v49, v3, s[8:9]
	v_cndmask_b32_e64 v3, v3, v48, s[8:9]
	v_cvt_pk_bf16_f32 v3, v3, v6
	global_store_dword v[4:5], v3, off offset:64 nt
	v_cndmask_b32_e64 v3, v32, v33, s[8:9]
	s_nop 1
	v_mov_b32_dpp v3, v3 quad_perm:[1,0,3,2] row_mask:0xf bank_mask:0xf bound_ctrl:1
	v_cndmask_b32_e64 v6, v33, v3, s[8:9]
	v_cndmask_b32_e64 v3, v3, v32, s[8:9]
	v_cvt_pk_bf16_f32 v3, v3, v6
	global_store_dword v[4:5], v3, off offset:128 nt
	v_cndmask_b32_e64 v3, v64, v65, s[8:9]
	s_nop 1
	v_mov_b32_dpp v3, v3 quad_perm:[1,0,3,2] row_mask:0xf bank_mask:0xf bound_ctrl:1
	v_cndmask_b32_e64 v6, v65, v3, s[8:9]
	v_cndmask_b32_e64 v3, v3, v64, s[8:9]
	v_cvt_pk_bf16_f32 v3, v3, v6
	global_store_dword v[4:5], v3, off offset:192 nt
	v_mov_b32_e32 v3, s76
	s_barrier
	ds_read_b32 v3, v3
	s_waitcnt lgkmcnt(0)
	v_cmp_gt_i32_e32 vcc, s3, v3
	v_readfirstlane_b32 s2, v3
	s_cbranch_vccz .LBB0_755

; __device__ __forceinline__ unsigned pk2(float a, float b) { f32x2_t v = {a, b}; bf16x2_t r = __builtin_convertvector(v, bf16x2_t); return __builtin_bit_cast(unsigned, r); }
; template <bool MLA>
; __device__ __forceinline__ void attn_unit(const P& p, LAS unsigned char* lds, const int b, const int h, const int qb) {
;     ...
;     if (MLA) { if (hi == 0) al[r32] = 1.0f / l_run; asm volatile("s_waitcnt lgkmcnt(0)" ::: "memory"); }
;     char* Ob = (char*)(WSP(bf16_t, WS_MIXED) + (size_t)(b * SEQ + qw) * 2048 + (MLA ? 1024 : 0) + h * 128);
;     const bool odd = (r32 & 1) != 0;
;     const unsigned oo = (unsigned)((4 * hi * 2048 + r32) * 2) + (odd ? 4094u : 0u);
; #pragma unroll
;     for (int q = 0; q < 8; ++q) { const int ra = 2 * q, c = (ra & 3) + 8 * (ra >> 2); const float iva = MLA ? al[c + 4 * hi] : 1.f, ivb = MLA ? al[c + 1 + 4 * hi] : 1.f;
; #pragma unroll
;         for (int d0 = 0; d0 < 4; ++d0) { const float A = o[d0][ra] * iva, Bv = o[d0][ra + 1] * ivb;
;             const float snd = odd ? A : Bv;
;             const float rcv = __int_as_float(__builtin_amdgcn_update_dpp(0, __float_as_int(snd), 0xB1, 0xF, 0xF, true));
;             const unsigned w = odd ? pk2(rcv, Bv) : pk2(A, rcv);
;             *(unsigned*)(Ob + oo + (unsigned)((c * 2048 + d0 * 32) * 2)) = w; } }
.LBB0_862:
	s_or_b64 exec, exec, s[0:1]
	s_waitcnt lgkmcnt(0)
	v_add_u32_e32 v3, s91, v201
	ds_read_b128 v[6:9], v3
	ds_read_b128 v[10:13], v3 offset:32
	s_lshl_b64 s[0:1], s[82:83], 12
	s_add_u32 s0, s74, s0
	s_addc_u32 s1, s75, s1
	s_lshl_b32 s2, s90, 1
	s_add_u32 s0, s0, s2
	s_waitcnt lgkmcnt(1)
	v_mul_f32_e32 v16, v66, v6
	v_mul_f32_e32 v17, v67, v7
	s_addc_u32 s1, s1, 0
	v_cndmask_b32_e64 v66, v16, v17, s[6:7]
	v_lshl_add_u64 v[4:5], s[0:1], 0, v[186:187]
	s_mov_b64 s[0:1], 0x13740800
	v_mov_b32_dpp v66, v66 quad_perm:[1,0,3,2] row_mask:0xf bank_mask:0xf bound_ctrl:1
	v_lshl_add_u64 v[14:15], v[4:5], 0, s[0:1]
	v_cndmask_b32_e64 v17, v17, v66, s[6:7]
	v_cndmask_b32_e64 v16, v66, v16, s[6:7]
	s_mov_b32 s0, 0x13740000
	v_cvt_pk_bf16_f32 v66, v16, v17
	v_add_co_u32_e32 v16, vcc, s0, v4
	s_mov_b32 s0, 0x13742000
	s_nop 0
	v_addc_co_u32_e32 v17, vcc, 0, v5, vcc
	global_store_dword v[16:17], v66, off offset:2048 nt
	v_mul_f32_e32 v16, v50, v6
	v_mul_f32_e32 v17, v51, v7
	v_cndmask_b32_e64 v50, v16, v17, s[6:7]
	s_nop 1
	v_mov_b32_dpp v50, v50 quad_perm:[1,0,3,2] row_mask:0xf bank_mask:0xf bound_ctrl:1
	v_cndmask_b32_e64 v17, v17, v50, s[6:7]
	v_cndmask_b32_e64 v16, v50, v16, s[6:7]
	v_cvt_pk_bf16_f32 v16, v16, v17
	global_store_dword v[14:15], v16, off offset:64 nt
	v_mul_f32_e32 v16, v34, v6
	v_mul_f32_e32 v17, v35, v7
	v_cndmask_b32_e64 v34, v16, v17, s[6:7]
	v_mul_f32_e32 v6, v18, v6
	v_mul_f32_e32 v7, v19, v7
	v_mov_b32_dpp v34, v34 quad_perm:[1,0,3,2] row_mask:0xf bank_mask:0xf bound_ctrl:1
	v_cndmask_b32_e64 v17, v17, v34, s[6:7]
	v_cndmask_b32_e64 v16, v34, v16, s[6:7]
	v_cvt_pk_bf16_f32 v16, v16, v17
	global_store_dword v[14:15], v16, off offset:128 nt
	v_cndmask_b32_e64 v16, v6, v7, s[6:7]
	s_nop 1
	v_mov_b32_dpp v16, v16 quad_perm:[1,0,3,2] row_mask:0xf bank_mask:0xf bound_ctrl:1
	v_cndmask_b32_e64 v7, v7, v16, s[6:7]
	v_cndmask_b32_e64 v6, v16, v6, s[6:7]
	v_cvt_pk_bf16_f32 v6, v6, v7
	global_store_dword v[14:15], v6, off offset:192 nt
	v_mul_f32_e32 v6, v68, v8
	v_mul_f32_e32 v7, v69, v9
	v_cndmask_b32_e64 v14, v6, v7, s[6:7]
	v_mul_f32_e32 v15, v53, v9
	s_nop 0
	v_mov_b32_dpp v14, v14 quad_perm:[1,0,3,2] row_mask:0xf bank_mask:0xf bound_ctrl:1
	v_cndmask_b32_e64 v7, v7, v14, s[6:7]
	v_cndmask_b32_e64 v6, v14, v6, s[6:7]
	v_cvt_pk_bf16_f32 v14, v6, v7
	v_add_co_u32_e32 v6, vcc, s0, v4
	s_mov_b32 s0, 0x13748000
	s_nop 0
	v_addc_co_u32_e32 v7, vcc, 0, v5, vcc
	global_store_dword v[6:7], v14, off offset:2048 nt
	v_mul_f32_e32 v14, v52, v8
	v_cndmask_b32_e64 v16, v14, v15, s[6:7]
	s_nop 1
	v_mov_b32_dpp v16, v16 quad_perm:[1,0,3,2] row_mask:0xf bank_mask:0xf bound_ctrl:1
	v_cndmask_b32_e64 v15, v15, v16, s[6:7]
	v_cndmask_b32_e64 v14, v16, v14, s[6:7]
	v_cvt_pk_bf16_f32 v14, v14, v15
	global_store_dword v[6:7], v14, off offset:2112 nt
	v_mul_f32_e32 v14, v36, v8
	v_mul_f32_e32 v15, v37, v9
	v_cndmask_b32_e64 v16, v14, v15, s[6:7]
	v_mul_f32_e32 v8, v20, v8
	v_mul_f32_e32 v9, v21, v9
	v_mov_b32_dpp v16, v16 quad_perm:[1,0,3,2] row_mask:0xf bank_mask:0xf bound_ctrl:1
	v_cndmask_b32_e64 v15, v15, v16, s[6:7]
	v_cndmask_b32_e64 v14, v16, v14, s[6:7]
	v_cvt_pk_bf16_f32 v14, v14, v15
	global_store_dword v[6:7], v14, off offset:2176 nt
	v_cndmask_b32_e64 v14, v8, v9, s[6:7]
	s_nop 1
	v_mov_b32_dpp v14, v14 quad_perm:[1,0,3,2] row_mask:0xf bank_mask:0xf bound_ctrl:1
	v_cndmask_b32_e64 v9, v9, v14, s[6:7]
	v_cndmask_b32_e64 v8, v14, v8, s[6:7]
	v_cvt_pk_bf16_f32 v8, v8, v9
	global_store_dword v[6:7], v8, off offset:2240 nt
	s_waitcnt lgkmcnt(0)
	v_mul_f32_e32 v6, v70, v10
	v_mul_f32_e32 v7, v71, v11
	v_cndmask_b32_e64 v8, v6, v7, s[6:7]
	v_mul_f32_e32 v9, v55, v11
	s_nop 0
	v_mov_b32_dpp v8, v8 quad_perm:[1,0,3,2] row_mask:0xf bank_mask:0xf bound_ctrl:1
	v_cndmask_b32_e64 v7, v7, v8, s[6:7]
	v_cndmask_b32_e64 v6, v8, v6, s[6:7]
	v_cvt_pk_bf16_f32 v8, v6, v7
	v_add_co_u32_e32 v6, vcc, s0, v4
	s_mov_b32 s0, 0x1374a000
	s_nop 0
	v_addc_co_u32_e32 v7, vcc, 0, v5, vcc
	global_store_dword v[6:7], v8, off offset:2048 nt
	v_mul_f32_e32 v8, v54, v10
	v_cndmask_b32_e64 v14, v8, v9, s[6:7]
	s_nop 1
	v_mov_b32_dpp v14, v14 quad_perm:[1,0,3,2] row_mask:0xf bank_mask:0xf bound_ctrl:1
	v_cndmask_b32_e64 v9, v9, v14, s[6:7]
	v_cndmask_b32_e64 v8, v14, v8, s[6:7]
	v_cvt_pk_bf16_f32 v8, v8, v9
	global_store_dword v[6:7], v8, off offset:2112 nt
	v_mul_f32_e32 v8, v38, v10
	v_mul_f32_e32 v9, v39, v11
	v_cndmask_b32_e64 v14, v8, v9, s[6:7]
	s_nop 1
	v_mov_b32_dpp v14, v14 quad_perm:[1,0,3,2] row_mask:0xf bank_mask:0xf bound_ctrl:1
	v_cndmask_b32_e64 v9, v9, v14, s[6:7]
	v_cndmask_b32_e64 v8, v14, v8, s[6:7]
	v_cvt_pk_bf16_f32 v8, v8, v9
	global_store_dword v[6:7], v8, off offset:2176 nt
	v_mul_f32_e32 v8, v22, v10
	v_mul_f32_e32 v9, v23, v11
	v_cndmask_b32_e64 v10, v8, v9, s[6:7]
	s_nop 1
	v_mov_b32_dpp v10, v10 quad_perm:[1,0,3,2] row_mask:0xf bank_mask:0xf bound_ctrl:1
	v_cndmask_b32_e64 v9, v9, v10, s[6:7]
	v_cndmask_b32_e64 v8, v10, v8, s[6:7]
	v_cvt_pk_bf16_f32 v8, v8, v9
	global_store_dword v[6:7], v8, off offset:2240 nt
	v_mul_f32_e32 v6, v72, v12
	v_mul_f32_e32 v7, v73, v13
	v_cndmask_b32_e64 v8, v6, v7, s[6:7]
	v_add_co_u32_e32 v10, vcc, s0, v4
	s_nop 0
	v_mov_b32_dpp v8, v8 quad_perm:[1,0,3,2] row_mask:0xf bank_mask:0xf bound_ctrl:1
	v_cndmask_b32_e64 v7, v7, v8, s[6:7]
	v_cndmask_b32_e64 v6, v8, v6, s[6:7]
	v_cvt_pk_bf16_f32 v6, v6, v7
	v_addc_co_u32_e32 v11, vcc, 0, v5, vcc
	global_store_dword v[10:11], v6, off offset:2048 nt
	v_mul_f32_e32 v6, v56, v12
	v_mul_f32_e32 v7, v57, v13
	v_cndmask_b32_e64 v8, v6, v7, s[6:7]
	s_mov_b32 s0, 0x13750000
	s_nop 0
	v_mov_b32_dpp v8, v8 quad_perm:[1,0,3,2] row_mask:0xf bank_mask:0xf bound_ctrl:1
	v_cndmask_b32_e64 v7, v7, v8, s[6:7]
	v_cndmask_b32_e64 v6, v8, v6, s[6:7]
	v_cvt_pk_bf16_f32 v6, v6, v7
	global_store_dword v[10:11], v6, off offset:2112 nt
	v_mul_f32_e32 v6, v40, v12
	v_mul_f32_e32 v7, v41, v13
	v_cndmask_b32_e64 v8, v6, v7, s[6:7]
	v_mul_f32_e32 v12, v24, v12
	s_nop 0
	v_mov_b32_dpp v8, v8 quad_perm:[1,0,3,2] row_mask:0xf bank_mask:0xf bound_ctrl:1
	v_cndmask_b32_e64 v7, v7, v8, s[6:7]
	v_cndmask_b32_e64 v6, v8, v6, s[6:7]
	v_cvt_pk_bf16_f32 v6, v6, v7
	global_store_dword v[10:11], v6, off offset:2176 nt
	v_mul_f32_e32 v6, v25, v13
	v_cndmask_b32_e64 v7, v12, v6, s[6:7]
	s_nop 1
	v_mov_b32_dpp v13, v7 quad_perm:[1,0,3,2] row_mask:0xf bank_mask:0xf bound_ctrl:1
	v_cndmask_b32_e64 v14, v6, v13, s[6:7]
	ds_read_b128 v[6:9], v3 offset:64
	v_cndmask_b32_e64 v12, v13, v12, s[6:7]
	v_cvt_pk_bf16_f32 v12, v12, v14
	global_store_dword v[10:11], v12, off offset:2240 nt
	ds_read_b128 v[10:13], v3 offset:96
	s_waitcnt lgkmcnt(1)
; __device__ __forceinline__ unsigned pk2(float a, float b) { f32x2_t v = {a, b}; bf16x2_t r = __builtin_convertvector(v, bf16x2_t); return __builtin_bit_cast(unsigned, r); }
; template <bool MLA>
; __device__ __forceinline__ void attn_unit(const P& p, LAS unsigned char* lds, const int b, const int h, const int qb) {
;     ...
; #pragma unroll
;     for (int q = 0; q < 8; ++q) { const int ra = 2 * q, c = (ra & 3) + 8 * (ra >> 2); const float iva = MLA ? al[c + 4 * hi] : 1.f, ivb = MLA ? al[c + 1 + 4 * hi] : 1.f;
; #pragma unroll
;         for (int d0 = 0; d0 < 4; ++d0) { const float A = o[d0][ra] * iva, Bv = o[d0][ra + 1] * ivb;
;             const float snd = odd ? A : Bv;
;             const float rcv = __int_as_float(__builtin_amdgcn_update_dpp(0, __float_as_int(snd), 0xB1, 0xF, 0xF, true));
;             const unsigned w = odd ? pk2(rcv, Bv) : pk2(A, rcv);
;             *(unsigned*)(Ob + oo + (unsigned)((c * 2048 + d0 * 32) * 2)) = w; } }
;     __syncthreads();
; __device__ __forceinline__ void attn_queues(const P& p, LAS unsigned char* lds, int* ctr, const int xg) {
;     ...
;             v = qs[0];
	v_mul_f32_e32 v3, v74, v6
	v_mul_f32_e32 v14, v75, v7
	v_cndmask_b32_e64 v15, v3, v14, s[6:7]
	v_mul_f32_e32 v16, v59, v7
	s_nop 0
	v_mov_b32_dpp v15, v15 quad_perm:[1,0,3,2] row_mask:0xf bank_mask:0xf bound_ctrl:1
	v_cndmask_b32_e64 v14, v14, v15, s[6:7]
	v_cndmask_b32_e64 v3, v15, v3, s[6:7]
	v_cvt_pk_bf16_f32 v3, v3, v14
	v_add_co_u32_e32 v14, vcc, s0, v4
	s_mov_b32 s0, 0x13752000
	s_nop 0
	v_addc_co_u32_e32 v15, vcc, 0, v5, vcc
	global_store_dword v[14:15], v3, off offset:2048 nt
	v_mul_f32_e32 v3, v58, v6
	v_cndmask_b32_e64 v17, v3, v16, s[6:7]
	s_nop 1
	v_mov_b32_dpp v17, v17 quad_perm:[1,0,3,2] row_mask:0xf bank_mask:0xf bound_ctrl:1
	v_cndmask_b32_e64 v16, v16, v17, s[6:7]
	v_cndmask_b32_e64 v3, v17, v3, s[6:7]
	v_cvt_pk_bf16_f32 v3, v3, v16
	global_store_dword v[14:15], v3, off offset:2112 nt
	v_mul_f32_e32 v3, v42, v6
	v_mul_f32_e32 v16, v43, v7
	v_cndmask_b32_e64 v17, v3, v16, s[6:7]
	s_nop 1
	v_mov_b32_dpp v17, v17 quad_perm:[1,0,3,2] row_mask:0xf bank_mask:0xf bound_ctrl:1
	v_cndmask_b32_e64 v16, v16, v17, s[6:7]
	v_cndmask_b32_e64 v3, v17, v3, s[6:7]
	v_cvt_pk_bf16_f32 v3, v3, v16
	global_store_dword v[14:15], v3, off offset:2176 nt
	v_mul_f32_e32 v3, v26, v6
	v_mul_f32_e32 v6, v27, v7
	v_cndmask_b32_e64 v7, v3, v6, s[6:7]
	s_nop 1
	v_mov_b32_dpp v7, v7 quad_perm:[1,0,3,2] row_mask:0xf bank_mask:0xf bound_ctrl:1
	v_cndmask_b32_e64 v6, v6, v7, s[6:7]
	v_cndmask_b32_e64 v3, v7, v3, s[6:7]
	v_cvt_pk_bf16_f32 v3, v3, v6
	global_store_dword v[14:15], v3, off offset:2240 nt
	v_mul_f32_e32 v3, v76, v8
	v_mul_f32_e32 v6, v77, v9
	v_cndmask_b32_e64 v7, v3, v6, s[6:7]
	v_mul_f32_e32 v14, v61, v9
	s_nop 0
	v_mov_b32_dpp v7, v7 quad_perm:[1,0,3,2] row_mask:0xf bank_mask:0xf bound_ctrl:1
	v_cndmask_b32_e64 v6, v6, v7, s[6:7]
	v_cndmask_b32_e64 v3, v7, v3, s[6:7]
	v_cvt_pk_bf16_f32 v3, v3, v6
	v_add_co_u32_e32 v6, vcc, s0, v4
	s_mov_b32 s0, 0x13758000
	s_nop 0
	v_addc_co_u32_e32 v7, vcc, 0, v5, vcc
	global_store_dword v[6:7], v3, off offset:2048 nt
	v_mul_f32_e32 v3, v60, v8
	v_cndmask_b32_e64 v15, v3, v14, s[6:7]
	s_nop 1
	v_mov_b32_dpp v15, v15 quad_perm:[1,0,3,2] row_mask:0xf bank_mask:0xf bound_ctrl:1
	v_cndmask_b32_e64 v14, v14, v15, s[6:7]
	v_cndmask_b32_e64 v3, v15, v3, s[6:7]
	v_cvt_pk_bf16_f32 v3, v3, v14
	global_store_dword v[6:7], v3, off offset:2112 nt
	v_mul_f32_e32 v3, v44, v8
	v_mul_f32_e32 v14, v45, v9
	v_cndmask_b32_e64 v15, v3, v14, s[6:7]
	s_nop 1
	v_mov_b32_dpp v15, v15 quad_perm:[1,0,3,2] row_mask:0xf bank_mask:0xf bound_ctrl:1
	v_cndmask_b32_e64 v14, v14, v15, s[6:7]
	v_cndmask_b32_e64 v3, v15, v3, s[6:7]
	v_cvt_pk_bf16_f32 v3, v3, v14
	global_store_dword v[6:7], v3, off offset:2176 nt
	v_mul_f32_e32 v3, v28, v8
	v_mul_f32_e32 v8, v29, v9
	v_cndmask_b32_e64 v9, v3, v8, s[6:7]
	s_nop 1
	v_mov_b32_dpp v9, v9 quad_perm:[1,0,3,2] row_mask:0xf bank_mask:0xf bound_ctrl:1
	v_cndmask_b32_e64 v8, v8, v9, s[6:7]
	v_cndmask_b32_e64 v3, v9, v3, s[6:7]
	v_cvt_pk_bf16_f32 v3, v3, v8
	global_store_dword v[6:7], v3, off offset:2240 nt
	s_waitcnt lgkmcnt(0)
	v_mul_f32_e32 v3, v78, v10
	v_mul_f32_e32 v6, v79, v11
	v_cndmask_b32_e64 v7, v3, v6, s[6:7]
	v_mul_f32_e32 v8, v63, v11
	s_nop 0
	v_mov_b32_dpp v7, v7 quad_perm:[1,0,3,2] row_mask:0xf bank_mask:0xf bound_ctrl:1
	v_cndmask_b32_e64 v6, v6, v7, s[6:7]
	v_cndmask_b32_e64 v3, v7, v3, s[6:7]
	v_cvt_pk_bf16_f32 v3, v3, v6
	v_add_co_u32_e32 v6, vcc, s0, v4
	s_mov_b32 s0, 0x1375a000
	s_nop 0
	v_addc_co_u32_e32 v7, vcc, 0, v5, vcc
	global_store_dword v[6:7], v3, off offset:2048 nt
	v_mul_f32_e32 v3, v62, v10
	v_cndmask_b32_e64 v9, v3, v8, s[6:7]
	v_add_co_u32_e32 v4, vcc, s0, v4
	s_nop 0
	v_mov_b32_dpp v9, v9 quad_perm:[1,0,3,2] row_mask:0xf bank_mask:0xf bound_ctrl:1
	v_cndmask_b32_e64 v8, v8, v9, s[6:7]
	v_cndmask_b32_e64 v3, v9, v3, s[6:7]
	v_cvt_pk_bf16_f32 v3, v3, v8
	global_store_dword v[6:7], v3, off offset:2112 nt
	v_mul_f32_e32 v3, v46, v10
	v_mul_f32_e32 v8, v47, v11
	v_cndmask_b32_e64 v9, v3, v8, s[6:7]
	v_addc_co_u32_e32 v5, vcc, 0, v5, vcc
	s_nop 0
	v_mov_b32_dpp v9, v9 quad_perm:[1,0,3,2] row_mask:0xf bank_mask:0xf bound_ctrl:1
	v_cndmask_b32_e64 v8, v8, v9, s[6:7]
	v_cndmask_b32_e64 v3, v9, v3, s[6:7]
	v_cvt_pk_bf16_f32 v3, v3, v8
	global_store_dword v[6:7], v3, off offset:2176 nt
	v_mul_f32_e32 v3, v30, v10
	v_mul_f32_e32 v8, v31, v11
	v_cndmask_b32_e64 v9, v3, v8, s[6:7]
	s_nop 1
	v_mov_b32_dpp v9, v9 quad_perm:[1,0,3,2] row_mask:0xf bank_mask:0xf bound_ctrl:1
	v_cndmask_b32_e64 v8, v8, v9, s[6:7]
	v_cndmask_b32_e64 v3, v9, v3, s[6:7]
	v_cvt_pk_bf16_f32 v3, v3, v8
	global_store_dword v[6:7], v3, off offset:2240 nt
	v_mul_f32_e32 v3, v80, v12
	v_mul_f32_e32 v6, v81, v13
	v_cndmask_b32_e64 v7, v3, v6, s[6:7]
	s_nop 1
	v_mov_b32_dpp v7, v7 quad_perm:[1,0,3,2] row_mask:0xf bank_mask:0xf bound_ctrl:1
	v_cndmask_b32_e64 v6, v6, v7, s[6:7]
	v_cndmask_b32_e64 v3, v7, v3, s[6:7]
	v_cvt_pk_bf16_f32 v3, v3, v6
	global_store_dword v[4:5], v3, off offset:2048 nt
	v_mul_f32_e32 v3, v64, v12
	v_mul_f32_e32 v6, v65, v13
	v_cndmask_b32_e64 v7, v3, v6, s[6:7]
	s_nop 1
	v_mov_b32_dpp v7, v7 quad_perm:[1,0,3,2] row_mask:0xf bank_mask:0xf bound_ctrl:1
	v_cndmask_b32_e64 v6, v6, v7, s[6:7]
	v_cndmask_b32_e64 v3, v7, v3, s[6:7]
	v_cvt_pk_bf16_f32 v3, v3, v6
	global_store_dword v[4:5], v3, off offset:2112 nt
	v_mul_f32_e32 v3, v48, v12
	v_mul_f32_e32 v6, v49, v13
	v_cndmask_b32_e64 v7, v3, v6, s[6:7]
	s_nop 1
	v_mov_b32_dpp v7, v7 quad_perm:[1,0,3,2] row_mask:0xf bank_mask:0xf bound_ctrl:1
	v_cndmask_b32_e64 v6, v6, v7, s[6:7]
	v_cndmask_b32_e64 v3, v7, v3, s[6:7]
	v_cvt_pk_bf16_f32 v3, v3, v6
	global_store_dword v[4:5], v3, off offset:2176 nt
	v_mul_f32_e32 v3, v32, v12
	v_mul_f32_e32 v6, v33, v13
	v_cndmask_b32_e64 v7, v3, v6, s[6:7]
	s_nop 1
	v_mov_b32_dpp v7, v7 quad_perm:[1,0,3,2] row_mask:0xf bank_mask:0xf bound_ctrl:1
	v_cndmask_b32_e64 v6, v6, v7, s[6:7]
	v_cndmask_b32_e64 v3, v7, v3, s[6:7]
	v_cvt_pk_bf16_f32 v3, v3, v6
	global_store_dword v[4:5], v3, off offset:2240 nt
	v_mov_b32_e32 v3, s40
	s_barrier
	ds_read_b32 v3, v3
	s_waitcnt lgkmcnt(0)
	v_cmp_gt_i32_e32 vcc, s3, v3
	v_readfirstlane_b32 s2, v3
	s_cbranch_vccz .LBB0_888

; __device__ __forceinline__ unsigned pk2(float a, float b) { f32x2_t v = {a, b}; bf16x2_t r = __builtin_convertvector(v, bf16x2_t); return __builtin_bit_cast(unsigned, r); }
; template <bool MLA>
; __device__ __forceinline__ void attn_unit(const P& p, LAS unsigned char* lds, const int b, const int h, const int qb) {
;     ...
;     char* Ob = (char*)(WSP(bf16_t, WS_MIXED) + (size_t)(b * SEQ + qw) * 2048 + (MLA ? 1024 : 0) + h * 128);
;     const bool odd = (r32 & 1) != 0;
;     const unsigned oo = (unsigned)((4 * hi * 2048 + r32) * 2) + (odd ? 4094u : 0u);
; #pragma unroll
;     for (int q = 0; q < 8; ++q) { const int ra = 2 * q, c = (ra & 3) + 8 * (ra >> 2); const float iva = MLA ? al[c + 4 * hi] : 1.f, ivb = MLA ? al[c + 1 + 4 * hi] : 1.f;
; #pragma unroll
;         for (int d0 = 0; d0 < 4; ++d0) { const float A = o[d0][ra] * iva, Bv = o[d0][ra + 1] * ivb;
;             const float snd = odd ? A : Bv;
;             const float rcv = __int_as_float(__builtin_amdgcn_update_dpp(0, __float_as_int(snd), 0xB1, 0xF, 0xF, true));
;             const unsigned w = odd ? pk2(rcv, Bv) : pk2(A, rcv);
;             *(unsigned*)(Ob + oo + (unsigned)((c * 2048 + d0 * 32) * 2)) = w; } }
;     __syncthreads();
.LBB0_895:
	s_lshl_b64 s[0:1], s[96:97], 12
	s_add_u32 s0, s90, s0
	s_addc_u32 s1, s91, s1
	v_cndmask_b32_e64 v3, v66, v67, s[8:9]
	s_add_u32 s0, s0, s2
	s_addc_u32 s1, s1, 0
	v_mov_b32_dpp v3, v3 quad_perm:[1,0,3,2] row_mask:0xf bank_mask:0xf bound_ctrl:1
	v_cndmask_b32_e64 v6, v67, v3, s[8:9]
	v_cndmask_b32_e64 v3, v3, v66, s[8:9]
	v_lshl_add_u64 v[4:5], s[0:1], 0, v[176:177]
	v_cvt_pk_bf16_f32 v3, v3, v6
	s_barrier
	global_store_dword v[4:5], v3, off nt
	v_cndmask_b32_e64 v3, v34, v35, s[8:9]
	s_movk_i32 s0, 0x2000
	s_mov_b32 s20, 0x10000
	v_mov_b32_dpp v3, v3 quad_perm:[1,0,3,2] row_mask:0xf bank_mask:0xf bound_ctrl:1
	v_cndmask_b32_e64 v6, v35, v3, s[8:9]
	v_cndmask_b32_e64 v3, v3, v34, s[8:9]
	v_cvt_pk_bf16_f32 v3, v3, v6
	global_store_dword v[4:5], v3, off offset:64 nt
	v_cndmask_b32_e64 v3, v18, v19, s[8:9]
	s_nop 1
	v_mov_b32_dpp v3, v3 quad_perm:[1,0,3,2] row_mask:0xf bank_mask:0xf bound_ctrl:1
	v_cndmask_b32_e64 v6, v19, v3, s[8:9]
	v_cndmask_b32_e64 v3, v3, v18, s[8:9]
	v_cvt_pk_bf16_f32 v3, v3, v6
	global_store_dword v[4:5], v3, off offset:128 nt
	v_cndmask_b32_e64 v3, v50, v51, s[8:9]
	s_nop 1
	v_mov_b32_dpp v3, v3 quad_perm:[1,0,3,2] row_mask:0xf bank_mask:0xf bound_ctrl:1
	v_cndmask_b32_e64 v6, v51, v3, s[8:9]
	v_cndmask_b32_e64 v3, v3, v50, s[8:9]
	v_cvt_pk_bf16_f32 v3, v3, v6
	global_store_dword v[4:5], v3, off offset:192 nt
	v_cndmask_b32_e64 v3, v68, v69, s[8:9]
	s_nop 1
	v_mov_b32_dpp v3, v3 quad_perm:[1,0,3,2] row_mask:0xf bank_mask:0xf bound_ctrl:1
	v_cndmask_b32_e64 v6, v69, v3, s[8:9]
	v_cndmask_b32_e64 v3, v3, v68, s[8:9]
	v_cvt_pk_bf16_f32 v3, v3, v6
	v_add_co_u32_e32 v6, vcc, s0, v4
	s_mov_b32 s0, 0x8000
	s_nop 0
	v_addc_co_u32_e32 v7, vcc, 0, v5, vcc
	global_store_dword v[6:7], v3, off nt
	v_cndmask_b32_e64 v3, v36, v37, s[8:9]
	s_nop 1
	v_mov_b32_dpp v3, v3 quad_perm:[1,0,3,2] row_mask:0xf bank_mask:0xf bound_ctrl:1
	v_cndmask_b32_e64 v8, v37, v3, s[8:9]
	v_cndmask_b32_e64 v3, v3, v36, s[8:9]
	v_cvt_pk_bf16_f32 v3, v3, v8
	global_store_dword v[6:7], v3, off offset:64 nt
	v_cndmask_b32_e64 v3, v20, v21, s[8:9]
	s_nop 1
	v_mov_b32_dpp v3, v3 quad_perm:[1,0,3,2] row_mask:0xf bank_mask:0xf bound_ctrl:1
	v_cndmask_b32_e64 v8, v21, v3, s[8:9]
	v_cndmask_b32_e64 v3, v3, v20, s[8:9]
	v_cvt_pk_bf16_f32 v3, v3, v8
	global_store_dword v[6:7], v3, off offset:128 nt
	v_cndmask_b32_e64 v3, v52, v53, s[8:9]
	s_nop 1
	v_mov_b32_dpp v3, v3 quad_perm:[1,0,3,2] row_mask:0xf bank_mask:0xf bound_ctrl:1
	v_cndmask_b32_e64 v8, v53, v3, s[8:9]
	v_cndmask_b32_e64 v3, v3, v52, s[8:9]
	v_cvt_pk_bf16_f32 v3, v3, v8
	global_store_dword v[6:7], v3, off offset:192 nt
	v_cndmask_b32_e64 v3, v70, v71, s[8:9]
	s_nop 1
	v_mov_b32_dpp v3, v3 quad_perm:[1,0,3,2] row_mask:0xf bank_mask:0xf bound_ctrl:1
	v_cndmask_b32_e64 v6, v71, v3, s[8:9]
	v_cndmask_b32_e64 v3, v3, v70, s[8:9]
	v_cvt_pk_bf16_f32 v3, v3, v6
	v_add_co_u32_e32 v6, vcc, s0, v4
	s_mov_b32 s0, 0xa000
	s_nop 0
	v_addc_co_u32_e32 v7, vcc, 0, v5, vcc
	global_store_dword v[6:7], v3, off nt
	v_cndmask_b32_e64 v3, v38, v39, s[8:9]
	s_nop 1
	v_mov_b32_dpp v3, v3 quad_perm:[1,0,3,2] row_mask:0xf bank_mask:0xf bound_ctrl:1
	v_cndmask_b32_e64 v8, v39, v3, s[8:9]
	v_cndmask_b32_e64 v3, v3, v38, s[8:9]
	v_cvt_pk_bf16_f32 v3, v3, v8
	global_store_dword v[6:7], v3, off offset:64 nt
	v_cndmask_b32_e64 v3, v22, v23, s[8:9]
	s_nop 1
	v_mov_b32_dpp v3, v3 quad_perm:[1,0,3,2] row_mask:0xf bank_mask:0xf bound_ctrl:1
	v_cndmask_b32_e64 v8, v23, v3, s[8:9]
	v_cndmask_b32_e64 v3, v3, v22, s[8:9]
	v_cvt_pk_bf16_f32 v3, v3, v8
	global_store_dword v[6:7], v3, off offset:128 nt
	v_cndmask_b32_e64 v3, v54, v55, s[8:9]
	s_nop 1
	v_mov_b32_dpp v3, v3 quad_perm:[1,0,3,2] row_mask:0xf bank_mask:0xf bound_ctrl:1
	v_cndmask_b32_e64 v8, v55, v3, s[8:9]
	v_cndmask_b32_e64 v3, v3, v54, s[8:9]
	v_cvt_pk_bf16_f32 v3, v3, v8
	global_store_dword v[6:7], v3, off offset:192 nt
	v_cndmask_b32_e64 v3, v72, v73, s[8:9]
	s_nop 1
	v_mov_b32_dpp v3, v3 quad_perm:[1,0,3,2] row_mask:0xf bank_mask:0xf bound_ctrl:1
	v_cndmask_b32_e64 v6, v73, v3, s[8:9]
	v_cndmask_b32_e64 v3, v3, v72, s[8:9]
	v_cvt_pk_bf16_f32 v3, v3, v6
	v_add_co_u32_e32 v6, vcc, s0, v4
	s_mov_b32 s0, 0x12000
	s_nop 0
	v_addc_co_u32_e32 v7, vcc, 0, v5, vcc
	global_store_dword v[6:7], v3, off nt
	v_cndmask_b32_e64 v3, v40, v41, s[8:9]
	s_nop 1
	v_mov_b32_dpp v3, v3 quad_perm:[1,0,3,2] row_mask:0xf bank_mask:0xf bound_ctrl:1
	v_cndmask_b32_e64 v8, v41, v3, s[8:9]
	v_cndmask_b32_e64 v3, v3, v40, s[8:9]
	v_cvt_pk_bf16_f32 v3, v3, v8
	global_store_dword v[6:7], v3, off offset:64 nt
	v_cndmask_b32_e64 v3, v24, v25, s[8:9]
	s_nop 1
	v_mov_b32_dpp v3, v3 quad_perm:[1,0,3,2] row_mask:0xf bank_mask:0xf bound_ctrl:1
	v_cndmask_b32_e64 v8, v25, v3, s[8:9]
	v_cndmask_b32_e64 v3, v3, v24, s[8:9]
	v_cvt_pk_bf16_f32 v3, v3, v8
	global_store_dword v[6:7], v3, off offset:128 nt
	v_cndmask_b32_e64 v3, v56, v57, s[8:9]
	s_nop 1
	v_mov_b32_dpp v3, v3 quad_perm:[1,0,3,2] row_mask:0xf bank_mask:0xf bound_ctrl:1
	v_cndmask_b32_e64 v8, v57, v3, s[8:9]
	v_cndmask_b32_e64 v3, v3, v56, s[8:9]
	v_cvt_pk_bf16_f32 v3, v3, v8
	global_store_dword v[6:7], v3, off offset:192 nt
; __device__ __forceinline__ unsigned pk2(float a, float b) { f32x2_t v = {a, b}; bf16x2_t r = __builtin_convertvector(v, bf16x2_t); return __builtin_bit_cast(unsigned, r); }
; template <bool MLA>
; __device__ __forceinline__ void attn_unit(const P& p, LAS unsigned char* lds, const int b, const int h, const int qb) {
;     ...
; #pragma unroll
;     for (int q = 0; q < 8; ++q) { const int ra = 2 * q, c = (ra & 3) + 8 * (ra >> 2); const float iva = MLA ? al[c + 4 * hi] : 1.f, ivb = MLA ? al[c + 1 + 4 * hi] : 1.f;
; #pragma unroll
;         for (int d0 = 0; d0 < 4; ++d0) { const float A = o[d0][ra] * iva, Bv = o[d0][ra + 1] * ivb;
;             const float snd = odd ? A : Bv;
;             const float rcv = __int_as_float(__builtin_amdgcn_update_dpp(0, __float_as_int(snd), 0xB1, 0xF, 0xF, true));
;             const unsigned w = odd ? pk2(rcv, Bv) : pk2(A, rcv);
;             *(unsigned*)(Ob + oo + (unsigned)((c * 2048 + d0 * 32) * 2)) = w; } }
;     __syncthreads();
; __device__ __forceinline__ void attn_queues(const P& p, LAS unsigned char* lds, int* ctr, const int xg) {
;     ...
;             v = qs[0];
	v_cndmask_b32_e64 v3, v74, v75, s[8:9]
	s_nop 1
	v_mov_b32_dpp v3, v3 quad_perm:[1,0,3,2] row_mask:0xf bank_mask:0xf bound_ctrl:1
	v_cndmask_b32_e64 v6, v75, v3, s[8:9]
	v_cndmask_b32_e64 v3, v3, v74, s[8:9]
	v_cvt_pk_bf16_f32 v3, v3, v6
	v_add_co_u32_e32 v6, vcc, s20, v4
	s_nop 1
	v_addc_co_u32_e32 v7, vcc, 0, v5, vcc
	global_store_dword v[6:7], v3, off nt
	v_cndmask_b32_e64 v3, v42, v43, s[8:9]
	s_nop 1
	v_mov_b32_dpp v3, v3 quad_perm:[1,0,3,2] row_mask:0xf bank_mask:0xf bound_ctrl:1
	v_cndmask_b32_e64 v8, v43, v3, s[8:9]
	v_cndmask_b32_e64 v3, v3, v42, s[8:9]
	v_cvt_pk_bf16_f32 v3, v3, v8
	global_store_dword v[6:7], v3, off offset:64 nt
	v_cndmask_b32_e64 v3, v26, v27, s[8:9]
	s_nop 1
	v_mov_b32_dpp v3, v3 quad_perm:[1,0,3,2] row_mask:0xf bank_mask:0xf bound_ctrl:1
	v_cndmask_b32_e64 v8, v27, v3, s[8:9]
	v_cndmask_b32_e64 v3, v3, v26, s[8:9]
	v_cvt_pk_bf16_f32 v3, v3, v8
	global_store_dword v[6:7], v3, off offset:128 nt
	v_cndmask_b32_e64 v3, v58, v59, s[8:9]
	s_nop 1
	v_mov_b32_dpp v3, v3 quad_perm:[1,0,3,2] row_mask:0xf bank_mask:0xf bound_ctrl:1
	v_cndmask_b32_e64 v8, v59, v3, s[8:9]
	v_cndmask_b32_e64 v3, v3, v58, s[8:9]
	v_cvt_pk_bf16_f32 v3, v3, v8
	global_store_dword v[6:7], v3, off offset:192 nt
	v_cndmask_b32_e64 v3, v76, v77, s[8:9]
	s_nop 1
	v_mov_b32_dpp v3, v3 quad_perm:[1,0,3,2] row_mask:0xf bank_mask:0xf bound_ctrl:1
	v_cndmask_b32_e64 v6, v77, v3, s[8:9]
	v_cndmask_b32_e64 v3, v3, v76, s[8:9]
	v_cvt_pk_bf16_f32 v3, v3, v6
	v_add_co_u32_e32 v6, vcc, s0, v4
	s_mov_b32 s0, 0x18000
	s_nop 0
	v_addc_co_u32_e32 v7, vcc, 0, v5, vcc
	global_store_dword v[6:7], v3, off nt
	v_cndmask_b32_e64 v3, v44, v45, s[8:9]
	s_nop 1
	v_mov_b32_dpp v3, v3 quad_perm:[1,0,3,2] row_mask:0xf bank_mask:0xf bound_ctrl:1
	v_cndmask_b32_e64 v8, v45, v3, s[8:9]
	v_cndmask_b32_e64 v3, v3, v44, s[8:9]
	v_cvt_pk_bf16_f32 v3, v3, v8
	global_store_dword v[6:7], v3, off offset:64 nt
	v_cndmask_b32_e64 v3, v28, v29, s[8:9]
	s_nop 1
	v_mov_b32_dpp v3, v3 quad_perm:[1,0,3,2] row_mask:0xf bank_mask:0xf bound_ctrl:1
	v_cndmask_b32_e64 v8, v29, v3, s[8:9]
	v_cndmask_b32_e64 v3, v3, v28, s[8:9]
	v_cvt_pk_bf16_f32 v3, v3, v8
	global_store_dword v[6:7], v3, off offset:128 nt
	v_cndmask_b32_e64 v3, v60, v61, s[8:9]
	s_nop 1
	v_mov_b32_dpp v3, v3 quad_perm:[1,0,3,2] row_mask:0xf bank_mask:0xf bound_ctrl:1
	v_cndmask_b32_e64 v8, v61, v3, s[8:9]
	v_cndmask_b32_e64 v3, v3, v60, s[8:9]
	v_cvt_pk_bf16_f32 v3, v3, v8
	global_store_dword v[6:7], v3, off offset:192 nt
	v_cndmask_b32_e64 v3, v78, v79, s[8:9]
	s_nop 1
	v_mov_b32_dpp v3, v3 quad_perm:[1,0,3,2] row_mask:0xf bank_mask:0xf bound_ctrl:1
	v_cndmask_b32_e64 v6, v79, v3, s[8:9]
	v_cndmask_b32_e64 v3, v3, v78, s[8:9]
	v_cvt_pk_bf16_f32 v3, v3, v6
	v_add_co_u32_e32 v6, vcc, s0, v4
	s_mov_b32 s0, 0x1a000
	s_nop 0
	v_addc_co_u32_e32 v7, vcc, 0, v5, vcc
	global_store_dword v[6:7], v3, off nt
	v_cndmask_b32_e64 v3, v46, v47, s[8:9]
	v_add_co_u32_e32 v4, vcc, s0, v4
	s_nop 0
	v_mov_b32_dpp v3, v3 quad_perm:[1,0,3,2] row_mask:0xf bank_mask:0xf bound_ctrl:1
	v_cndmask_b32_e64 v8, v47, v3, s[8:9]
	v_cndmask_b32_e64 v3, v3, v46, s[8:9]
	v_cvt_pk_bf16_f32 v3, v3, v8
	global_store_dword v[6:7], v3, off offset:64 nt
	v_cndmask_b32_e64 v3, v30, v31, s[8:9]
	v_addc_co_u32_e32 v5, vcc, 0, v5, vcc
	s_nop 0
	v_mov_b32_dpp v3, v3 quad_perm:[1,0,3,2] row_mask:0xf bank_mask:0xf bound_ctrl:1
	v_cndmask_b32_e64 v8, v31, v3, s[8:9]
	v_cndmask_b32_e64 v3, v3, v30, s[8:9]
	v_cvt_pk_bf16_f32 v3, v3, v8
	global_store_dword v[6:7], v3, off offset:128 nt
	v_cndmask_b32_e64 v3, v62, v63, s[8:9]
	s_nop 1
	v_mov_b32_dpp v3, v3 quad_perm:[1,0,3,2] row_mask:0xf bank_mask:0xf bound_ctrl:1
	v_cndmask_b32_e64 v8, v63, v3, s[8:9]
	v_cndmask_b32_e64 v3, v3, v62, s[8:9]
	v_cvt_pk_bf16_f32 v3, v3, v8
	global_store_dword v[6:7], v3, off offset:192 nt
	v_cndmask_b32_e64 v3, v80, v81, s[8:9]
	s_nop 1
	v_mov_b32_dpp v3, v3 quad_perm:[1,0,3,2] row_mask:0xf bank_mask:0xf bound_ctrl:1
	v_cndmask_b32_e64 v6, v81, v3, s[8:9]
	v_cndmask_b32_e64 v3, v3, v80, s[8:9]
	v_cvt_pk_bf16_f32 v3, v3, v6
	global_store_dword v[4:5], v3, off nt
	v_cndmask_b32_e64 v3, v48, v49, s[8:9]
	s_nop 1
	v_mov_b32_dpp v3, v3 quad_perm:[1,0,3,2] row_mask:0xf bank_mask:0xf bound_ctrl:1
	v_cndmask_b32_e64 v6, v49, v3, s[8:9]
	v_cndmask_b32_e64 v3, v3, v48, s[8:9]
	v_cvt_pk_bf16_f32 v3, v3, v6
	global_store_dword v[4:5], v3, off offset:64 nt
	v_cndmask_b32_e64 v3, v32, v33, s[8:9]
	s_nop 1
	v_mov_b32_dpp v3, v3 quad_perm:[1,0,3,2] row_mask:0xf bank_mask:0xf bound_ctrl:1
	v_cndmask_b32_e64 v6, v33, v3, s[8:9]
	v_cndmask_b32_e64 v3, v3, v32, s[8:9]
	v_cvt_pk_bf16_f32 v3, v3, v6
	global_store_dword v[4:5], v3, off offset:128 nt
	v_cndmask_b32_e64 v3, v64, v65, s[8:9]
	s_nop 1
	v_mov_b32_dpp v3, v3 quad_perm:[1,0,3,2] row_mask:0xf bank_mask:0xf bound_ctrl:1
	v_cndmask_b32_e64 v6, v65, v3, s[8:9]
	v_cndmask_b32_e64 v3, v3, v64, s[8:9]
	v_cvt_pk_bf16_f32 v3, v3, v6
	global_store_dword v[4:5], v3, off offset:192 nt
	v_mov_b32_e32 v3, s76
	s_barrier
	ds_read_b32 v3, v3
	s_waitcnt lgkmcnt(0)
	v_cmp_gt_i32_e32 vcc, s3, v3
	v_readfirstlane_b32 s2, v3
	s_cbranch_vccz .LBB0_921
